# SB attention 1+e adds and final multiplies packed (v_pk_add/v_pk_mul), SwiGLU epilogue 128 scalar multiplies packed into 64 v_pk_mul_f32, on top of MLA packed exp section
# speedup vs baseline: 1.0117x; 1.0044x over previous
.LBB0_305:
	v_add_u32_e32 v173, 0, v71
	v_add_u32_e32 v172, 0x121c0, v173
	v_add_u32_e32 v175, 0x121d0, v173
	s_waitcnt lgkmcnt(3)
	v_mfma_f32_32x32x16_bf16 v[34:49], v[200:203], v[50:53], 0
	s_mov_b64 s[54:55], -1
	s_waitcnt lgkmcnt(2)
	v_mfma_f32_32x32x16_bf16 v[34:49], v[204:207], v[54:57], v[34:49]
	s_waitcnt lgkmcnt(1)
	v_mfma_f32_32x32x16_bf16 v[34:49], v[208:211], v[58:61], v[34:49]
	s_waitcnt lgkmcnt(0)
	v_mfma_f32_32x32x16_bf16 v[34:49], v[212:215], v[62:65], v[34:49]
	v_add_u32_e32 v76, 0xffffee00, v67
	v_max_i32_e32 v76, 0, v76
	ds_read_b128 v[200:203], v76
	ds_read_b128 v[204:207], v76 offset:32
	ds_read_b128 v[208:211], v76 offset:64
	ds_read_b128 v[212:215], v76 offset:96
	s_nop 5
	v_pk_mul_f32 v[46:47], v[46:47], s[88:89] op_sel_hi:[1,0]
	v_pk_mul_f32 v[48:49], v[48:49], s[88:89] op_sel_hi:[1,0]
	v_min_f32_e32 v47, 0x42700000, v47
	v_pk_mul_f32 v[44:45], v[44:45], s[88:89] op_sel_hi:[1,0]
	v_exp_f32_e32 v151, v47
	v_min_f32_e32 v47, 0x42700000, v48
	v_min_f32_e32 v44, 0x42700000, v44
	v_exp_f32_e32 v152, v47
	v_min_f32_e32 v47, 0x42700000, v49
	v_exp_f32_e32 v148, v44
	v_min_f32_e32 v44, 0x42700000, v45
	v_exp_f32_e32 v153, v47
	v_exp_f32_e32 v149, v44
	v_min_f32_e32 v44, 0x42700000, v46
	v_pk_mul_f32 v[42:43], v[42:43], s[88:89] op_sel_hi:[1,0]
	v_exp_f32_e32 v150, v44
	v_min_f32_e32 v42, 0x42700000, v42
	v_exp_f32_e32 v80, v42
	v_min_f32_e32 v42, 0x42700000, v43
	v_pk_add_f32 v[48:49], v[152:153], 1.0 op_sel_hi:[1,0]
	v_pk_mul_f32 v[40:41], v[40:41], s[88:89] op_sel_hi:[1,0]
	v_exp_f32_e32 v81, v42
	v_rcp_f32_e32 v48, v48
	v_rcp_f32_e32 v155, v49
	v_min_f32_e32 v41, 0x42700000, v41
	v_pk_add_f32 v[46:47], v[150:151], 1.0 op_sel_hi:[1,0]
	v_rcp_f32_e32 v47, v47
	v_pk_mul_f32 v[38:39], v[38:39], s[88:89] op_sel_hi:[1,0]
	v_min_f32_e32 v40, 0x42700000, v40
	v_exp_f32_e32 v79, v41
	v_rcp_f32_e32 v46, v46
	v_min_f32_e32 v39, 0x42700000, v39
	v_exp_f32_e32 v78, v40
	v_pk_add_f32 v[44:45], v[148:149], 1.0 op_sel_hi:[1,0]
	v_rcp_f32_e32 v45, v45
	v_pk_mul_f32 v[36:37], v[36:37], s[88:89] op_sel_hi:[1,0]
	v_min_f32_e32 v38, 0x42700000, v38
	v_exp_f32_e32 v77, v39
	v_rcp_f32_e32 v44, v44
	v_mul_f32_e32 v154, v48, v155
	v_min_f32_e32 v37, 0x42700000, v37
	v_exp_f32_e32 v76, v38
	v_pk_add_f32 v[42:43], v[80:81], 1.0 op_sel_hi:[1,0]
	v_rcp_f32_e32 v43, v43
	v_mul_f32_e32 v159, v47, v154
	v_pk_mul_f32 v[34:35], v[34:35], s[88:89] op_sel_hi:[1,0]
	v_min_f32_e32 v36, 0x42700000, v36
	v_exp_f32_e32 v75, v37
	v_rcp_f32_e32 v42, v42
	v_mul_f32_e32 v158, v46, v159
	v_min_f32_e32 v35, 0x42700000, v35
	v_exp_f32_e32 v74, v36
	v_pk_add_f32 v[40:41], v[78:79], 1.0 op_sel_hi:[1,0]
	v_rcp_f32_e32 v41, v41
	v_mul_f32_e32 v161, v45, v158
	v_min_f32_e32 v34, 0x42700000, v34
	v_exp_f32_e32 v73, v35
	v_rcp_f32_e32 v40, v40
	v_mul_f32_e32 v160, v44, v161
	v_exp_f32_e32 v72, v34
	v_pk_add_f32 v[38:39], v[76:77], 1.0 op_sel_hi:[1,0]
	v_rcp_f32_e32 v39, v39
	v_mul_f32_e32 v163, v43, v160
	v_rcp_f32_e32 v38, v38
	v_mul_f32_e32 v162, v42, v163
	v_pk_add_f32 v[36:37], v[74:75], 1.0 op_sel_hi:[1,0]
	v_rcp_f32_e32 v37, v37
	v_mul_f32_e32 v43, v41, v162
	v_rcp_f32_e32 v36, v36
	v_mul_f32_e32 v42, v40, v43
	v_pk_add_f32 v[34:35], v[72:73], 1.0 op_sel_hi:[1,0]
	v_rcp_f32_e32 v35, v35
	v_mul_f32_e32 v45, v39, v42
	v_rcp_f32_e32 v34, v34
	v_mul_f32_e32 v44, v38, v45
	v_mul_f32_e32 v47, v37, v44
	v_mul_f32_e32 v46, v36, v47
	v_mul_f32_e32 v165, v35, v46
	v_mul_f32_e32 v164, v34, v165
	ds_bpermute_b32 v174, v156, v164
	ds_read_b128 v[34:37], v172
	v_add_u32_e32 v38, 0x1a5c0, v173
	ds_read_b128 v[38:41], v38
	s_waitcnt lgkmcnt(2)
	v_cndmask_b32_e64 v48, 1.0, v174, s[36:37]
	v_mul_f32_e32 v172, v157, v48
	v_pk_mul_f32 v[48:49], v[172:173], v[164:165] op_sel_hi:[0,1]
	v_pk_mul_f32 v[46:47], v[172:173], v[46:47] op_sel_hi:[0,1]
	v_pk_mul_f32 v[44:45], v[172:173], v[44:45] op_sel_hi:[0,1]
	v_pk_mul_f32 v[42:43], v[172:173], v[42:43] op_sel_hi:[0,1]
	v_pk_mul_f32 v[48:49], v[72:73], v[48:49]
	v_pk_mul_f32 v[46:47], v[74:75], v[46:47]
	v_pk_mul_f32 v[44:45], v[76:77], v[44:45]
	v_pk_mul_f32 v[72:73], v[78:79], v[42:43]
	v_cvt_pk_bf16_f32 v42, v48, v49
	v_cvt_pk_bf16_f32 v43, v46, v47
	v_cvt_pk_bf16_f32 v44, v44, v45
	v_cvt_pk_bf16_f32 v45, v72, v73
	ds_read_b128 v[46:49], v175
	v_pk_mul_f32 v[76:77], v[172:173], v[158:159] op_sel_hi:[0,1]
	s_waitcnt lgkmcnt(2)
	v_mfma_f32_32x32x16_bf16 v[2:17], v[34:37], v[42:45], v[2:17]
	v_pk_mul_f32 v[34:35], v[172:173], v[162:163] op_sel_hi:[0,1]
	v_add_u32_e32 v36, 0x1a5d0, v173
	v_pk_mul_f32 v[72:73], v[80:81], v[34:35]
	v_pk_mul_f32 v[34:35], v[172:173], v[160:161] op_sel_hi:[0,1]
	v_pk_mul_f32 v[74:75], v[148:149], v[34:35]
	ds_read_b128 v[34:37], v36
	s_waitcnt lgkmcnt(2)
	v_mfma_f32_32x32x16_bf16 v[18:33], v[38:41], v[42:45], v[18:33]
	v_pk_mul_f32 v[38:39], v[172:173], v[154:155] op_sel_hi:[0,1]
	v_pk_mul_f32 v[40:41], v[150:151], v[76:77]
	v_pk_mul_f32 v[42:43], v[152:153], v[38:39]
	v_cvt_pk_bf16_f32 v38, v72, v73
	v_cvt_pk_bf16_f32 v39, v74, v75
	v_cvt_pk_bf16_f32 v40, v40, v41
	v_cvt_pk_bf16_f32 v41, v42, v43
	v_mul_f32_e32 v42, v164, v174
	v_mul_f32_e32 v157, v157, v42
	s_waitcnt lgkmcnt(1)
	v_mfma_f32_32x32x16_bf16 v[2:17], v[46:49], v[38:41], v[2:17]
	v_cmp_eq_f32_e32 vcc, 0, v157
	s_cmp_eq_u64 vcc, exec
	s_waitcnt lgkmcnt(0)
	v_mfma_f32_32x32x16_bf16 v[18:33], v[34:37], v[38:41], v[18:33]
	s_cbranch_scc0 .LBB0_304
	s_mov_b64 s[52:53], -1
	s_branch .LBB0_309

.LBB0_313:
	v_lshl_add_u64 v[34:35], s[78:79], 0, v[150:151]
	v_add_co_u32_e32 v74, vcc, 0x8200000, v34
	s_cmp_eq_u32 s50, s42
	s_nop 0
	v_addc_co_u32_e32 v75, vcc, 0, v35, vcc
	global_load_dwordx4 v[34:37], v[74:75], off offset:2048
	global_load_dwordx4 v[66:69], v[74:75], off offset:2080
	global_load_dwordx4 v[70:73], v[74:75], off offset:2112
	global_load_dwordx4 v[152:155], v[74:75], off offset:2144
	v_lshl_add_u64 v[74:75], s[78:79], 0, v[148:149]
	s_cselect_b64 s[46:47], -1, 0
	s_cmp_lg_u32 s50, s42
	s_waitcnt vmcnt(3)
	v_mfma_f32_32x32x16_bf16 v[34:49], v[34:37], v[50:53], 0
	s_waitcnt vmcnt(2)
	v_mfma_f32_32x32x16_bf16 v[34:49], v[66:69], v[54:57], v[34:49]
	v_add_co_u32_e32 v66, vcc, 0xc200000, v74
	s_nop 1
	v_addc_co_u32_e32 v67, vcc, 0, v75, vcc
	v_add_co_u32_e32 v158, vcc, 0xc300000, v74
	s_waitcnt vmcnt(1)
	v_mfma_f32_32x32x16_bf16 v[34:49], v[70:73], v[58:61], v[34:49]
	v_addc_co_u32_e32 v159, vcc, 0, v75, vcc
	global_load_dwordx4 v[78:81], v[66:67], off
	s_nop 0
	global_load_dwordx4 v[66:69], v[66:67], off offset:16
	s_nop 0
	global_load_dwordx4 v[74:77], v[158:159], off
	global_load_dwordx4 v[70:73], v[158:159], off offset:16
	s_waitcnt vmcnt(4)
	v_mfma_f32_32x32x16_bf16 v[34:49], v[152:155], v[62:65], v[34:49]
	s_nop 11
	v_pk_mul_f32 v[48:49], v[48:49], s[88:89] op_sel_hi:[1,0]
	v_pk_mul_f32 v[46:47], v[46:47], s[88:89] op_sel_hi:[1,0]
	v_pk_mul_f32 v[44:45], v[44:45], s[88:89] op_sel_hi:[1,0]
	v_pk_mul_f32 v[42:43], v[42:43], s[88:89] op_sel_hi:[1,0]
	v_pk_mul_f32 v[40:41], v[40:41], s[88:89] op_sel_hi:[1,0]
	v_pk_mul_f32 v[38:39], v[38:39], s[88:89] op_sel_hi:[1,0]
	v_pk_mul_f32 v[36:37], v[36:37], s[88:89] op_sel_hi:[1,0]
	v_pk_mul_f32 v[34:35], v[34:35], s[88:89] op_sel_hi:[1,0]
	v_min_f32_e32 v36, 0x42700000, v36
	v_min_f32_e32 v34, 0x42700000, v34
	v_min_f32_e32 v35, 0x42700000, v35
	v_min_f32_e32 v37, 0x42700000, v37
	v_min_f32_e32 v38, 0x42700000, v38
	v_min_f32_e32 v39, 0x42700000, v39
	v_min_f32_e32 v40, 0x42700000, v40
	v_min_f32_e32 v41, 0x42700000, v41
	v_min_f32_e32 v152, 0x42700000, v42
	v_min_f32_e32 v153, 0x42700000, v43
	v_min_f32_e32 v154, 0x42700000, v44
	v_min_f32_e32 v155, 0x42700000, v45
	v_min_f32_e32 v158, 0x42700000, v46
	v_min_f32_e32 v159, 0x42700000, v47
	v_min_f32_e32 v160, 0x42700000, v48
	v_min_f32_e32 v161, 0x42700000, v49
	v_exp_f32_e32 v44, v34
	v_exp_f32_e32 v45, v35
	v_exp_f32_e32 v46, v36
	v_exp_f32_e32 v47, v37
	v_exp_f32_e32 v48, v38
	v_exp_f32_e32 v49, v39
	v_exp_f32_e32 v42, v40
	v_exp_f32_e32 v43, v41
	v_exp_f32_e32 v40, v152
	v_exp_f32_e32 v41, v153
	v_exp_f32_e32 v38, v154
	v_exp_f32_e32 v39, v155
	v_exp_f32_e32 v36, v158
	v_exp_f32_e32 v37, v159
	v_exp_f32_e32 v34, v160
	v_exp_f32_e32 v35, v161
	v_pk_add_f32 v[152:153], v[44:45], 1.0 op_sel_hi:[1,0]
	v_pk_add_f32 v[158:159], v[46:47], 1.0 op_sel_hi:[1,0]
	v_pk_add_f32 v[160:161], v[48:49], 1.0 op_sel_hi:[1,0]
	v_pk_add_f32 v[162:163], v[42:43], 1.0 op_sel_hi:[1,0]
	v_pk_add_f32 v[164:165], v[40:41], 1.0 op_sel_hi:[1,0]
	v_pk_add_f32 v[172:173], v[38:39], 1.0 op_sel_hi:[1,0]
	v_pk_add_f32 v[174:175], v[36:37], 1.0 op_sel_hi:[1,0]
	v_pk_add_f32 v[176:177], v[34:35], 1.0 op_sel_hi:[1,0]
	v_rcp_f32_e32 v154, v152
	v_rcp_f32_e32 v155, v153
	v_rcp_f32_e32 v158, v158
	v_rcp_f32_e32 v159, v159
	v_rcp_f32_e32 v160, v160
	v_rcp_f32_e32 v161, v161
	v_rcp_f32_e32 v162, v162
	v_rcp_f32_e32 v163, v163
	v_rcp_f32_e32 v164, v164
	v_rcp_f32_e32 v165, v165
	v_rcp_f32_e32 v172, v172
	v_rcp_f32_e32 v173, v173
	v_rcp_f32_e32 v174, v174
	v_rcp_f32_e32 v175, v175
	v_rcp_f32_e32 v152, v176
	v_rcp_f32_e32 v153, v177
	s_cbranch_scc1 .LBB0_315
	v_cndmask_b32_e64 v154, 1.0, v154, s[2:3]
	v_cndmask_b32_e64 v155, 1.0, v155, s[4:5]
	v_cndmask_b32_e64 v158, 1.0, v158, s[6:7]
	v_cndmask_b32_e64 v159, 1.0, v159, s[8:9]
	v_cndmask_b32_e64 v160, 1.0, v160, s[10:11]
	v_cndmask_b32_e64 v161, 1.0, v161, s[12:13]
	v_cndmask_b32_e64 v162, 1.0, v162, s[14:15]
	v_cndmask_b32_e64 v163, 1.0, v163, s[16:17]
	v_cndmask_b32_e64 v164, 1.0, v164, s[18:19]
	v_cndmask_b32_e64 v165, 1.0, v165, s[20:21]
	v_cndmask_b32_e64 v172, 1.0, v172, s[22:23]
	v_cndmask_b32_e64 v173, 1.0, v173, s[24:25]
	v_cndmask_b32_e64 v174, 1.0, v174, s[26:27]
	v_cndmask_b32_e64 v175, 1.0, v175, s[28:29]
	v_cndmask_b32_e64 v152, 1.0, v152, s[30:31]
	v_cndmask_b32_e64 v153, 1.0, v153, s[34:35]

.LBB0_783:
	s_mov_b32 s98, 0xc01d265f
	s_mov_b32 s100, 0xc0c00000
	v_mov_b32_e32 v203, 0x41000000
	s_add_i32 s2, 0, 0x20000
	s_nop 15
	s_nop 15
	v_add_u32_e32 v2, s2, v178
	ds_read_b128 v[10:13], v2
	v_readlane_b32 s3, v238, 9
	v_add_u32_e32 v18, s47, v175
	v_ashrrev_i32_e32 v19, 31, v18
	v_add_u32_e32 v6, s3, v179
	ds_read_b128 v[6:9], v6
	s_waitcnt lgkmcnt(0)
	v_pk_add_f32 v[24:25], v[158:159], v[10:11]
	v_pk_add_f32 v[22:23], v[160:161], v[12:13]
	v_min_f32_e32 v25, 0x40e00000, v25
	v_min_f32_e32 v24, 0x40e00000, v24
	v_pk_mul_f32 v[30:31], s[98:99], v[24:25] op_sel_hi:[0,1]
	v_min_f32_e32 v23, 0x40e00000, v23
	v_min_f32_e32 v22, 0x40e00000, v22
	v_exp_f32_e32 v30, v30
	v_exp_f32_e32 v31, v31
	v_add_u32_e32 v2, s3, v178
	v_pk_mul_f32 v[32:33], s[98:99], v[22:23] op_sel_hi:[0,1]
	ds_read_b128 v[14:17], v2
	v_exp_f32_e32 v32, v32
	v_exp_f32_e32 v33, v33
	v_pk_add_f32 v[30:31], v[30:31], 1.0 op_sel_hi:[1,0]
	v_add_u32_e32 v2, s2, v179
	v_rcp_f32_e32 v30, v30
	v_rcp_f32_e32 v31, v31
	v_pk_add_f32 v[32:33], v[32:33], 1.0 op_sel_hi:[1,0]
	s_waitcnt lgkmcnt(0)
	v_pk_add_f32 v[14:15], v[14:15], 1.0 op_sel_hi:[1,0]
	v_pk_add_f32 v[16:17], v[16:17], 1.0 op_sel_hi:[1,0]
	v_pk_add_f32 v[28:29], v[154:155], v[14:15]
	v_rcp_f32_e32 v32, v32
	v_rcp_f32_e32 v33, v33
	ds_read_b128 v[2:5], v2
	v_med3_f32 v28, v28, s100, v203
	v_pk_add_f32 v[26:27], v[156:157], v[16:17]
	v_med3_f32 v29, v29, s100, v203
	v_pk_mul_f32 v[24:25], v[24:25], v[30:31]
	v_med3_f32 v26, v26, s100, v203
	v_med3_f32 v27, v27, s100, v203
	v_pk_mul_f32 v[22:23], v[22:23], v[32:33]
	v_pk_mul_f32 v[154:155], v[28:29], v[24:25]
	v_pk_mul_f32 v[156:157], v[26:27], v[22:23]
	s_waitcnt lgkmcnt(0)
	v_pk_add_f32 v[22:23], v[152:153], v[4:5]
	v_pk_add_f32 v[24:25], v[150:151], v[2:3]
	v_min_f32_e32 v23, 0x40e00000, v23
	v_min_f32_e32 v22, 0x40e00000, v22
	v_min_f32_e32 v25, 0x40e00000, v25
	v_min_f32_e32 v24, 0x40e00000, v24
	v_pk_mul_f32 v[30:31], s[98:99], v[24:25] op_sel_hi:[0,1]
	v_pk_mul_f32 v[32:33], s[98:99], v[22:23] op_sel_hi:[0,1]
	v_exp_f32_e32 v30, v30
	v_exp_f32_e32 v31, v31
	v_exp_f32_e32 v32, v32
	v_exp_f32_e32 v33, v33
	v_pk_add_f32 v[6:7], v[6:7], 1.0 op_sel_hi:[1,0]
	v_pk_add_f32 v[8:9], v[8:9], 1.0 op_sel_hi:[1,0]
	v_pk_add_f32 v[26:27], v[148:149], v[8:9]
	v_pk_add_f32 v[30:31], v[30:31], 1.0 op_sel_hi:[1,0]
	v_pk_add_f32 v[28:29], v[146:147], v[6:7]
	v_pk_add_f32 v[32:33], v[32:33], 1.0 op_sel_hi:[1,0]
	v_rcp_f32_e32 v30, v30
	v_rcp_f32_e32 v31, v31
	v_rcp_f32_e32 v32, v32
	v_rcp_f32_e32 v33, v33
	v_med3_f32 v26, v26, s100, v203
	v_med3_f32 v28, v28, s100, v203
	v_med3_f32 v27, v27, s100, v203
	v_med3_f32 v29, v29, s100, v203
	v_pk_mul_f32 v[22:23], v[22:23], v[32:33]
	v_pk_mul_f32 v[24:25], v[24:25], v[30:31]
	v_pk_mul_f32 v[24:25], v[28:29], v[24:25]
	v_pk_mul_f32 v[26:27], v[26:27], v[22:23]
	v_cvt_pk_fp8_f32 v22, v154, v155
	v_cvt_pk_fp8_f32 v23, v24, v25
	v_add_u32_e32 v20, s48, v180
	v_lshlrev_b64 v[18:19], 10, v[18:19]
	v_cvt_pk_fp8_f32 v22, v156, v157 op_sel:[0,0,1]
	v_cvt_pk_fp8_f32 v23, v26, v27 op_sel:[0,0,1]
	v_ashrrev_i32_e32 v21, 31, v20
	v_lshl_add_u64 v[18:19], s[6:7], 0, v[18:19]
	v_lshl_add_u64 v[18:19], v[18:19], 0, v[20:21]
	flat_store_dwordx2 v[18:19], v[22:23]
	v_pk_add_f32 v[22:23], v[142:143], v[10:11]
	v_pk_add_f32 v[20:21], v[144:145], v[12:13]
	v_min_f32_e32 v23, 0x40e00000, v23
	v_min_f32_e32 v22, 0x40e00000, v22
	v_pk_mul_f32 v[28:29], s[98:99], v[22:23] op_sel_hi:[0,1]
	v_min_f32_e32 v21, 0x40e00000, v21
	v_min_f32_e32 v20, 0x40e00000, v20
	v_exp_f32_e32 v28, v28
	v_exp_f32_e32 v29, v29
	v_pk_mul_f32 v[30:31], s[98:99], v[20:21] op_sel_hi:[0,1]
	v_exp_f32_e32 v30, v30
	v_exp_f32_e32 v31, v31
	v_pk_add_f32 v[28:29], v[28:29], 1.0 op_sel_hi:[1,0]
	v_pk_add_f32 v[26:27], v[138:139], v[14:15]
	v_rcp_f32_e32 v28, v28
	v_rcp_f32_e32 v29, v29
	v_pk_add_f32 v[30:31], v[30:31], 1.0 op_sel_hi:[1,0]
	v_med3_f32 v26, v26, s100, v203
	v_rcp_f32_e32 v30, v30
	v_rcp_f32_e32 v31, v31
	v_pk_add_f32 v[24:25], v[140:141], v[16:17]
	v_med3_f32 v27, v27, s100, v203
	v_pk_mul_f32 v[22:23], v[22:23], v[28:29]
	v_med3_f32 v24, v24, s100, v203
	v_med3_f32 v25, v25, s100, v203
	v_pk_mul_f32 v[20:21], v[20:21], v[30:31]
	v_pk_mul_f32 v[32:33], v[26:27], v[22:23]
	v_pk_mul_f32 v[138:139], v[24:25], v[20:21]
	v_pk_add_f32 v[20:21], v[136:137], v[4:5]
	v_pk_add_f32 v[22:23], v[134:135], v[2:3]
	v_min_f32_e32 v21, 0x40e00000, v21
	v_min_f32_e32 v20, 0x40e00000, v20
	v_min_f32_e32 v23, 0x40e00000, v23
	v_min_f32_e32 v22, 0x40e00000, v22
	v_pk_mul_f32 v[28:29], s[98:99], v[22:23] op_sel_hi:[0,1]
	v_pk_mul_f32 v[30:31], s[98:99], v[20:21] op_sel_hi:[0,1]
	v_exp_f32_e32 v28, v28
	v_exp_f32_e32 v29, v29
	v_exp_f32_e32 v30, v30
	v_exp_f32_e32 v31, v31
	v_pk_add_f32 v[24:25], v[132:133], v[8:9]
	v_pk_add_f32 v[28:29], v[28:29], 1.0 op_sel_hi:[1,0]
	v_pk_add_f32 v[26:27], v[130:131], v[6:7]
	v_pk_add_f32 v[30:31], v[30:31], 1.0 op_sel_hi:[1,0]
	v_rcp_f32_e32 v28, v28
	v_rcp_f32_e32 v29, v29
	v_rcp_f32_e32 v30, v30
	v_rcp_f32_e32 v31, v31
	v_med3_f32 v24, v24, s100, v203
	v_med3_f32 v26, v26, s100, v203
	v_med3_f32 v25, v25, s100, v203
	v_med3_f32 v27, v27, s100, v203
	v_pk_mul_f32 v[20:21], v[20:21], v[30:31]
	v_pk_mul_f32 v[22:23], v[22:23], v[28:29]
	v_pk_mul_f32 v[22:23], v[26:27], v[22:23]
	v_pk_mul_f32 v[24:25], v[24:25], v[20:21]
	v_cvt_pk_fp8_f32 v20, v32, v33
	v_cvt_pk_fp8_f32 v21, v22, v23
	v_add_co_u32_e32 v22, vcc, s69, v18
	v_cvt_pk_fp8_f32 v20, v138, v139 op_sel:[0,0,1]
	v_cvt_pk_fp8_f32 v21, v24, v25 op_sel:[0,0,1]
	v_addc_co_u32_e32 v23, vcc, 0, v19, vcc
	v_pk_add_f32 v[26:27], v[122:123], v[14:15]
	flat_store_dwordx2 v[22:23], v[20:21]
	v_pk_add_f32 v[22:23], v[126:127], v[10:11]
	v_pk_add_f32 v[20:21], v[128:129], v[12:13]
	v_min_f32_e32 v23, 0x40e00000, v23
	v_min_f32_e32 v22, 0x40e00000, v22
	v_pk_mul_f32 v[28:29], s[98:99], v[22:23] op_sel_hi:[0,1]
	v_min_f32_e32 v21, 0x40e00000, v21
	v_min_f32_e32 v20, 0x40e00000, v20
	v_exp_f32_e32 v28, v28
	v_exp_f32_e32 v29, v29
	v_pk_mul_f32 v[30:31], s[98:99], v[20:21] op_sel_hi:[0,1]
	v_exp_f32_e32 v30, v30
	v_exp_f32_e32 v31, v31
	v_pk_add_f32 v[28:29], v[28:29], 1.0 op_sel_hi:[1,0]
	v_med3_f32 v26, v26, s100, v203
	v_rcp_f32_e32 v28, v28
	v_rcp_f32_e32 v29, v29
	v_pk_add_f32 v[30:31], v[30:31], 1.0 op_sel_hi:[1,0]
	v_pk_add_f32 v[24:25], v[124:125], v[16:17]
	v_rcp_f32_e32 v30, v30
	v_rcp_f32_e32 v31, v31
	v_med3_f32 v27, v27, s100, v203
	v_pk_mul_f32 v[22:23], v[22:23], v[28:29]
	v_med3_f32 v24, v24, s100, v203
	v_med3_f32 v25, v25, s100, v203
	v_pk_mul_f32 v[20:21], v[20:21], v[30:31]
	v_pk_mul_f32 v[32:33], v[26:27], v[22:23]
	v_pk_mul_f32 v[122:123], v[24:25], v[20:21]
	v_pk_add_f32 v[20:21], v[120:121], v[4:5]
	v_pk_add_f32 v[22:23], v[118:119], v[2:3]
	v_min_f32_e32 v21, 0x40e00000, v21
	v_min_f32_e32 v20, 0x40e00000, v20
	v_min_f32_e32 v23, 0x40e00000, v23
	v_min_f32_e32 v22, 0x40e00000, v22
	v_pk_mul_f32 v[28:29], s[98:99], v[22:23] op_sel_hi:[0,1]
	v_pk_mul_f32 v[30:31], s[98:99], v[20:21] op_sel_hi:[0,1]
	v_exp_f32_e32 v28, v28
	v_exp_f32_e32 v29, v29
	v_exp_f32_e32 v30, v30
	v_exp_f32_e32 v31, v31
	v_pk_add_f32 v[24:25], v[116:117], v[8:9]
	v_pk_add_f32 v[28:29], v[28:29], 1.0 op_sel_hi:[1,0]
	v_pk_add_f32 v[26:27], v[114:115], v[6:7]
	v_pk_add_f32 v[30:31], v[30:31], 1.0 op_sel_hi:[1,0]
	v_rcp_f32_e32 v28, v28
	v_rcp_f32_e32 v29, v29
	v_rcp_f32_e32 v30, v30
	v_rcp_f32_e32 v31, v31
	v_med3_f32 v24, v24, s100, v203
	v_med3_f32 v26, v26, s100, v203
	v_med3_f32 v25, v25, s100, v203
	v_med3_f32 v27, v27, s100, v203
	v_pk_mul_f32 v[20:21], v[20:21], v[30:31]
	v_pk_mul_f32 v[22:23], v[22:23], v[28:29]
	v_pk_mul_f32 v[22:23], v[26:27], v[22:23]
	v_pk_mul_f32 v[24:25], v[24:25], v[20:21]
	v_cvt_pk_fp8_f32 v20, v32, v33
	v_cvt_pk_fp8_f32 v21, v22, v23
	v_add_co_u32_e32 v22, vcc, s67, v18
	v_cvt_pk_fp8_f32 v20, v122, v123 op_sel:[0,0,1]
	v_cvt_pk_fp8_f32 v21, v24, v25 op_sel:[0,0,1]
	v_addc_co_u32_e32 v23, vcc, 0, v19, vcc
	v_pk_add_f32 v[26:27], v[106:107], v[14:15]
	flat_store_dwordx2 v[22:23], v[20:21]
	v_pk_add_f32 v[22:23], v[110:111], v[10:11]
	v_pk_add_f32 v[20:21], v[112:113], v[12:13]
	v_min_f32_e32 v23, 0x40e00000, v23
	v_min_f32_e32 v22, 0x40e00000, v22
	v_pk_mul_f32 v[28:29], s[98:99], v[22:23] op_sel_hi:[0,1]
	v_min_f32_e32 v21, 0x40e00000, v21
	v_min_f32_e32 v20, 0x40e00000, v20
	v_exp_f32_e32 v28, v28
	v_exp_f32_e32 v29, v29
	v_pk_mul_f32 v[30:31], s[98:99], v[20:21] op_sel_hi:[0,1]
	v_exp_f32_e32 v30, v30
	v_exp_f32_e32 v31, v31
	v_pk_add_f32 v[28:29], v[28:29], 1.0 op_sel_hi:[1,0]
	v_med3_f32 v26, v26, s100, v203
	v_rcp_f32_e32 v28, v28
	v_rcp_f32_e32 v29, v29
	v_pk_add_f32 v[30:31], v[30:31], 1.0 op_sel_hi:[1,0]
	v_pk_add_f32 v[24:25], v[108:109], v[16:17]
	v_rcp_f32_e32 v30, v30
	v_rcp_f32_e32 v31, v31
	v_med3_f32 v27, v27, s100, v203
	v_pk_mul_f32 v[22:23], v[22:23], v[28:29]
	v_med3_f32 v24, v24, s100, v203
	v_med3_f32 v25, v25, s100, v203
	v_pk_mul_f32 v[20:21], v[20:21], v[30:31]
	v_pk_mul_f32 v[32:33], v[26:27], v[22:23]
	v_pk_mul_f32 v[106:107], v[24:25], v[20:21]
	v_pk_add_f32 v[20:21], v[104:105], v[4:5]
	v_pk_add_f32 v[22:23], v[102:103], v[2:3]
	v_min_f32_e32 v21, 0x40e00000, v21
	v_min_f32_e32 v20, 0x40e00000, v20
	v_min_f32_e32 v23, 0x40e00000, v23
	v_min_f32_e32 v22, 0x40e00000, v22
	v_pk_mul_f32 v[28:29], s[98:99], v[22:23] op_sel_hi:[0,1]
	v_pk_mul_f32 v[30:31], s[98:99], v[20:21] op_sel_hi:[0,1]
	v_exp_f32_e32 v28, v28
	v_exp_f32_e32 v29, v29
	v_exp_f32_e32 v30, v30
	v_exp_f32_e32 v31, v31
	v_pk_add_f32 v[24:25], v[100:101], v[8:9]
	v_pk_add_f32 v[28:29], v[28:29], 1.0 op_sel_hi:[1,0]
	v_pk_add_f32 v[26:27], v[98:99], v[6:7]
	v_pk_add_f32 v[30:31], v[30:31], 1.0 op_sel_hi:[1,0]
	v_rcp_f32_e32 v28, v28
	v_rcp_f32_e32 v29, v29
	v_rcp_f32_e32 v30, v30
	v_rcp_f32_e32 v31, v31
	v_med3_f32 v24, v24, s100, v203
	v_med3_f32 v26, v26, s100, v203
	v_med3_f32 v25, v25, s100, v203
	v_med3_f32 v27, v27, s100, v203
	v_pk_mul_f32 v[20:21], v[20:21], v[30:31]
	v_pk_mul_f32 v[22:23], v[22:23], v[28:29]
	v_pk_mul_f32 v[22:23], v[26:27], v[22:23]
	v_pk_mul_f32 v[24:25], v[24:25], v[20:21]
	v_cvt_pk_fp8_f32 v20, v32, v33
	v_cvt_pk_fp8_f32 v21, v22, v23
	s_mov_b32 s2, 0xc000
	v_add_co_u32_e32 v22, vcc, s2, v18
	v_cvt_pk_fp8_f32 v20, v106, v107 op_sel:[0,0,1]
	v_cvt_pk_fp8_f32 v21, v24, v25 op_sel:[0,0,1]
	v_addc_co_u32_e32 v23, vcc, 0, v19, vcc
	v_pk_add_f32 v[26:27], v[90:91], v[14:15]
	flat_store_dwordx2 v[22:23], v[20:21]
	v_pk_add_f32 v[22:23], v[94:95], v[10:11]
	v_pk_add_f32 v[20:21], v[96:97], v[12:13]
	v_min_f32_e32 v23, 0x40e00000, v23
	v_min_f32_e32 v22, 0x40e00000, v22
	v_pk_mul_f32 v[28:29], s[98:99], v[22:23] op_sel_hi:[0,1]
	v_min_f32_e32 v21, 0x40e00000, v21
	v_min_f32_e32 v20, 0x40e00000, v20
	v_exp_f32_e32 v28, v28
	v_exp_f32_e32 v29, v29
	v_pk_mul_f32 v[30:31], s[98:99], v[20:21] op_sel_hi:[0,1]
	v_exp_f32_e32 v30, v30
	v_exp_f32_e32 v31, v31
	v_pk_add_f32 v[28:29], v[28:29], 1.0 op_sel_hi:[1,0]
	v_med3_f32 v26, v26, s100, v203
	v_rcp_f32_e32 v28, v28
	v_rcp_f32_e32 v29, v29
	v_pk_add_f32 v[30:31], v[30:31], 1.0 op_sel_hi:[1,0]
	v_pk_add_f32 v[24:25], v[92:93], v[16:17]
	v_rcp_f32_e32 v30, v30
	v_rcp_f32_e32 v31, v31
	v_med3_f32 v27, v27, s100, v203
	v_pk_mul_f32 v[22:23], v[22:23], v[28:29]
	v_med3_f32 v24, v24, s100, v203
	v_med3_f32 v25, v25, s100, v203
	v_pk_mul_f32 v[20:21], v[20:21], v[30:31]
	v_pk_mul_f32 v[32:33], v[26:27], v[22:23]
	v_pk_mul_f32 v[90:91], v[24:25], v[20:21]
	v_pk_add_f32 v[20:21], v[88:89], v[4:5]
	v_pk_add_f32 v[22:23], v[86:87], v[2:3]
	v_min_f32_e32 v21, 0x40e00000, v21
	v_min_f32_e32 v20, 0x40e00000, v20
	v_min_f32_e32 v23, 0x40e00000, v23
	v_min_f32_e32 v22, 0x40e00000, v22
	v_pk_mul_f32 v[28:29], s[98:99], v[22:23] op_sel_hi:[0,1]
	v_pk_mul_f32 v[30:31], s[98:99], v[20:21] op_sel_hi:[0,1]
	v_exp_f32_e32 v28, v28
	v_exp_f32_e32 v29, v29
	v_exp_f32_e32 v30, v30
	v_exp_f32_e32 v31, v31
	v_pk_add_f32 v[24:25], v[84:85], v[8:9]
	v_pk_add_f32 v[28:29], v[28:29], 1.0 op_sel_hi:[1,0]
	v_pk_add_f32 v[26:27], v[82:83], v[6:7]
	v_pk_add_f32 v[30:31], v[30:31], 1.0 op_sel_hi:[1,0]
	v_rcp_f32_e32 v28, v28
	v_rcp_f32_e32 v29, v29
	v_rcp_f32_e32 v30, v30
	v_rcp_f32_e32 v31, v31
	v_med3_f32 v24, v24, s100, v203
	v_med3_f32 v26, v26, s100, v203
	v_med3_f32 v25, v25, s100, v203
	v_med3_f32 v27, v27, s100, v203
	v_pk_mul_f32 v[20:21], v[20:21], v[30:31]
	v_pk_mul_f32 v[22:23], v[22:23], v[28:29]
	v_pk_mul_f32 v[22:23], v[26:27], v[22:23]
	v_pk_mul_f32 v[24:25], v[24:25], v[20:21]
	v_cvt_pk_fp8_f32 v20, v32, v33
	v_cvt_pk_fp8_f32 v21, v22, v23
	s_mov_b32 s2, 0x20000
	v_add_co_u32_e32 v22, vcc, s2, v18
	v_cvt_pk_fp8_f32 v20, v90, v91 op_sel:[0,0,1]
	v_cvt_pk_fp8_f32 v21, v24, v25 op_sel:[0,0,1]
	v_addc_co_u32_e32 v23, vcc, 0, v19, vcc
	v_pk_add_f32 v[26:27], v[74:75], v[14:15]
	flat_store_dwordx2 v[22:23], v[20:21]
	v_pk_add_f32 v[22:23], v[78:79], v[10:11]
	v_pk_add_f32 v[20:21], v[80:81], v[12:13]
	v_min_f32_e32 v23, 0x40e00000, v23
	v_min_f32_e32 v22, 0x40e00000, v22
	v_pk_mul_f32 v[28:29], s[98:99], v[22:23] op_sel_hi:[0,1]
	v_min_f32_e32 v21, 0x40e00000, v21
	v_min_f32_e32 v20, 0x40e00000, v20
	v_exp_f32_e32 v28, v28
	v_exp_f32_e32 v29, v29
	v_pk_mul_f32 v[30:31], s[98:99], v[20:21] op_sel_hi:[0,1]
	v_exp_f32_e32 v30, v30
	v_exp_f32_e32 v31, v31
	v_pk_add_f32 v[28:29], v[28:29], 1.0 op_sel_hi:[1,0]
	v_med3_f32 v26, v26, s100, v203
	v_rcp_f32_e32 v28, v28
	v_rcp_f32_e32 v29, v29
	v_pk_add_f32 v[30:31], v[30:31], 1.0 op_sel_hi:[1,0]
	v_pk_add_f32 v[24:25], v[76:77], v[16:17]
	v_rcp_f32_e32 v30, v30
	v_rcp_f32_e32 v31, v31
	v_med3_f32 v27, v27, s100, v203
	v_pk_mul_f32 v[22:23], v[22:23], v[28:29]
	v_med3_f32 v24, v24, s100, v203
	v_med3_f32 v25, v25, s100, v203
	v_pk_mul_f32 v[20:21], v[20:21], v[30:31]
	v_pk_mul_f32 v[32:33], v[26:27], v[22:23]
	v_pk_mul_f32 v[74:75], v[24:25], v[20:21]
	v_pk_add_f32 v[20:21], v[72:73], v[4:5]
	v_pk_add_f32 v[22:23], v[70:71], v[2:3]
	v_min_f32_e32 v21, 0x40e00000, v21
	v_min_f32_e32 v20, 0x40e00000, v20
	v_min_f32_e32 v23, 0x40e00000, v23
	v_min_f32_e32 v22, 0x40e00000, v22
	v_pk_mul_f32 v[28:29], s[98:99], v[22:23] op_sel_hi:[0,1]
	v_pk_mul_f32 v[30:31], s[98:99], v[20:21] op_sel_hi:[0,1]
	v_exp_f32_e32 v28, v28
	v_exp_f32_e32 v29, v29
	v_exp_f32_e32 v30, v30
	v_exp_f32_e32 v31, v31
	v_pk_add_f32 v[24:25], v[68:69], v[8:9]
	v_pk_add_f32 v[28:29], v[28:29], 1.0 op_sel_hi:[1,0]
	v_pk_add_f32 v[26:27], v[66:67], v[6:7]
	v_pk_add_f32 v[30:31], v[30:31], 1.0 op_sel_hi:[1,0]
	v_rcp_f32_e32 v28, v28
	v_rcp_f32_e32 v29, v29
	v_rcp_f32_e32 v30, v30
	v_rcp_f32_e32 v31, v31
	v_med3_f32 v24, v24, s100, v203
	v_med3_f32 v26, v26, s100, v203
	v_med3_f32 v25, v25, s100, v203
	v_med3_f32 v27, v27, s100, v203
	v_pk_mul_f32 v[20:21], v[20:21], v[30:31]
	v_pk_mul_f32 v[22:23], v[22:23], v[28:29]
	v_pk_mul_f32 v[22:23], v[26:27], v[22:23]
	v_pk_mul_f32 v[24:25], v[24:25], v[20:21]
	v_cvt_pk_fp8_f32 v20, v32, v33
	v_cvt_pk_fp8_f32 v21, v22, v23
	s_mov_b32 s2, 0x24000
	v_add_co_u32_e32 v22, vcc, s2, v18
	v_cvt_pk_fp8_f32 v20, v74, v75 op_sel:[0,0,1]
	v_cvt_pk_fp8_f32 v21, v24, v25 op_sel:[0,0,1]
	v_addc_co_u32_e32 v23, vcc, 0, v19, vcc
	v_pk_add_f32 v[26:27], v[58:59], v[14:15]
	flat_store_dwordx2 v[22:23], v[20:21]
	v_pk_add_f32 v[22:23], v[62:63], v[10:11]
	v_pk_add_f32 v[20:21], v[64:65], v[12:13]
	v_min_f32_e32 v23, 0x40e00000, v23
	v_min_f32_e32 v22, 0x40e00000, v22
	v_pk_mul_f32 v[28:29], s[98:99], v[22:23] op_sel_hi:[0,1]
	v_min_f32_e32 v21, 0x40e00000, v21
	v_min_f32_e32 v20, 0x40e00000, v20
	v_exp_f32_e32 v28, v28
	v_exp_f32_e32 v29, v29
	v_pk_mul_f32 v[30:31], s[98:99], v[20:21] op_sel_hi:[0,1]
	v_exp_f32_e32 v30, v30
	v_exp_f32_e32 v31, v31
	v_pk_add_f32 v[28:29], v[28:29], 1.0 op_sel_hi:[1,0]
	v_med3_f32 v26, v26, s100, v203
	v_rcp_f32_e32 v28, v28
	v_rcp_f32_e32 v29, v29
	v_pk_add_f32 v[30:31], v[30:31], 1.0 op_sel_hi:[1,0]
	v_pk_add_f32 v[24:25], v[60:61], v[16:17]
	v_rcp_f32_e32 v30, v30
	v_rcp_f32_e32 v31, v31
	v_med3_f32 v27, v27, s100, v203
	v_pk_mul_f32 v[22:23], v[22:23], v[28:29]
	v_med3_f32 v24, v24, s100, v203
	v_med3_f32 v25, v25, s100, v203
	v_pk_mul_f32 v[20:21], v[20:21], v[30:31]
	v_pk_mul_f32 v[32:33], v[26:27], v[22:23]
	v_pk_mul_f32 v[58:59], v[24:25], v[20:21]
	v_pk_add_f32 v[20:21], v[56:57], v[4:5]
	v_pk_add_f32 v[22:23], v[54:55], v[2:3]
	v_min_f32_e32 v21, 0x40e00000, v21
	v_min_f32_e32 v20, 0x40e00000, v20
	v_min_f32_e32 v23, 0x40e00000, v23
	v_min_f32_e32 v22, 0x40e00000, v22
	v_pk_mul_f32 v[28:29], s[98:99], v[22:23] op_sel_hi:[0,1]
	v_pk_mul_f32 v[30:31], s[98:99], v[20:21] op_sel_hi:[0,1]
	v_exp_f32_e32 v28, v28
	v_exp_f32_e32 v29, v29
	v_exp_f32_e32 v30, v30
	v_exp_f32_e32 v31, v31
	v_pk_add_f32 v[24:25], v[52:53], v[8:9]
	v_pk_add_f32 v[28:29], v[28:29], 1.0 op_sel_hi:[1,0]
	v_pk_add_f32 v[26:27], v[50:51], v[6:7]
	v_pk_add_f32 v[30:31], v[30:31], 1.0 op_sel_hi:[1,0]
	v_rcp_f32_e32 v28, v28
	v_rcp_f32_e32 v29, v29
	v_rcp_f32_e32 v30, v30
	v_rcp_f32_e32 v31, v31
	v_med3_f32 v24, v24, s100, v203
	v_med3_f32 v26, v26, s100, v203
	v_med3_f32 v25, v25, s100, v203
	v_med3_f32 v27, v27, s100, v203
	v_pk_mul_f32 v[20:21], v[20:21], v[30:31]
	v_pk_mul_f32 v[22:23], v[22:23], v[28:29]
	v_pk_mul_f32 v[22:23], v[26:27], v[22:23]
	v_pk_mul_f32 v[24:25], v[24:25], v[20:21]
	v_cvt_pk_fp8_f32 v20, v32, v33
	v_cvt_pk_fp8_f32 v21, v22, v23
	s_mov_b32 s2, 0x28000
	v_add_co_u32_e32 v22, vcc, s2, v18
	v_cvt_pk_fp8_f32 v20, v58, v59 op_sel:[0,0,1]
	v_cvt_pk_fp8_f32 v21, v24, v25 op_sel:[0,0,1]
	v_pk_add_f32 v[10:11], v[46:47], v[10:11]
	v_addc_co_u32_e32 v23, vcc, 0, v19, vcc
	v_min_f32_e32 v11, 0x40e00000, v11
	v_min_f32_e32 v10, 0x40e00000, v10
	flat_store_dwordx2 v[22:23], v[20:21]
	v_pk_add_f32 v[12:13], v[48:49], v[12:13]
	v_pk_mul_f32 v[20:21], s[98:99], v[10:11] op_sel_hi:[0,1]
	v_min_f32_e32 v13, 0x40e00000, v13
	v_min_f32_e32 v12, 0x40e00000, v12
	v_exp_f32_e32 v20, v20
	v_exp_f32_e32 v21, v21
	v_pk_mul_f32 v[22:23], s[98:99], v[12:13] op_sel_hi:[0,1]
	v_exp_f32_e32 v22, v22
	v_exp_f32_e32 v23, v23
	v_pk_add_f32 v[20:21], v[20:21], 1.0 op_sel_hi:[1,0]
	v_pk_add_f32 v[14:15], v[42:43], v[14:15]
	v_rcp_f32_e32 v20, v20
	v_rcp_f32_e32 v21, v21
	v_pk_add_f32 v[22:23], v[22:23], 1.0 op_sel_hi:[1,0]
	v_med3_f32 v14, v14, s100, v203
	v_rcp_f32_e32 v22, v22
	v_rcp_f32_e32 v23, v23
	v_pk_add_f32 v[16:17], v[44:45], v[16:17]
	v_med3_f32 v15, v15, s100, v203
	v_pk_mul_f32 v[10:11], v[10:11], v[20:21]
	v_med3_f32 v16, v16, s100, v203
	v_med3_f32 v17, v17, s100, v203
	v_pk_mul_f32 v[12:13], v[12:13], v[22:23]
	v_pk_mul_f32 v[14:15], v[14:15], v[10:11]
	v_pk_add_f32 v[2:3], v[38:39], v[2:3]
	v_min_f32_e32 v3, 0x40e00000, v3
	v_min_f32_e32 v2, 0x40e00000, v2
	v_pk_mul_f32 v[16:17], v[16:17], v[12:13]
	v_pk_add_f32 v[4:5], v[40:41], v[4:5]
	v_pk_mul_f32 v[10:11], s[98:99], v[2:3] op_sel_hi:[0,1]
	v_min_f32_e32 v5, 0x40e00000, v5
	v_min_f32_e32 v4, 0x40e00000, v4
	v_exp_f32_e32 v10, v10
	v_exp_f32_e32 v11, v11
	v_pk_mul_f32 v[12:13], s[98:99], v[4:5] op_sel_hi:[0,1]
	v_exp_f32_e32 v12, v12
	v_exp_f32_e32 v13, v13
	v_pk_add_f32 v[10:11], v[10:11], 1.0 op_sel_hi:[1,0]
	v_pk_add_f32 v[6:7], v[34:35], v[6:7]
	v_rcp_f32_e32 v10, v10
	v_rcp_f32_e32 v11, v11
	v_pk_add_f32 v[12:13], v[12:13], 1.0 op_sel_hi:[1,0]
	v_med3_f32 v6, v6, s100, v203
	v_rcp_f32_e32 v12, v12
	v_rcp_f32_e32 v13, v13
	v_pk_add_f32 v[8:9], v[36:37], v[8:9]
	v_med3_f32 v7, v7, s100, v203
	v_pk_mul_f32 v[2:3], v[2:3], v[10:11]
	v_med3_f32 v8, v8, s100, v203
	v_med3_f32 v9, v9, s100, v203
	v_pk_mul_f32 v[4:5], v[4:5], v[12:13]
	v_pk_mul_f32 v[6:7], v[6:7], v[2:3]
	v_pk_mul_f32 v[4:5], v[8:9], v[4:5]
	v_cvt_pk_fp8_f32 v2, v14, v15
	v_cvt_pk_fp8_f32 v3, v6, v7
	s_mov_b64 s[2:3], -1
	v_cvt_pk_fp8_f32 v2, v16, v17 op_sel:[0,0,1]
	v_cvt_pk_fp8_f32 v3, v4, v5 op_sel:[0,0,1]
	v_add_co_u32_e32 v4, vcc, 0x2c000, v18
	s_nop 1
	v_addc_co_u32_e32 v5, vcc, 0, v19, vcc
	s_andn2_b64 vcc, exec, s[14:15]
	flat_store_dwordx2 v[4:5], v[2:3]
	s_cbranch_vccnz .LBB0_772
	s_andn2_b64 vcc, exec, s[4:5]
	s_cbranch_vccnz .LBB0_771
	s_barrier
	s_branch .LBB0_771
